# v028
# speedup vs baseline: 1.0541x; 1.0045x over previous
.Ltok_done:
	v_cmp_ne_u32_e32 vcc, 0, v7
	s_and_saveexec_b64 s[6:7], vcc
	v_mov_b32_e32 v1, 1
	v_mov_b32_e32 v2, 0
	ds_write_b32 v2, v1 offset:24832
	s_or_b64 exec, exec, s[6:7]
	s_mov_b32 s5, 0
	s_cmp_eq_u32 s16, 0
	s_cselect_b64 vcc, -1, 0
	v_mov_b32_e32 v157, 0
	s_waitcnt lgkmcnt(0)
	s_barrier
	ds_read_b32 v1, v157 offset:24832
	v_lshrrev_b32_e32 v108, 6, v0
	v_and_b32_e32 v4, 63, v0
	s_movk_i32 s0, 0x1000
	v_mov_b32_e32 v9, v157
	s_waitcnt lgkmcnt(0)
	v_readfirstlane_b32 s4, v1
	v_lshl_or_b32 v1, s16, 3, v108
	v_mul_u32_u24_e32 v1, 0x300, v1
	v_lshlrev_b32_e32 v156, 4, v1
	v_lshl_add_u64 v[2:3], s[8:9], 0, v[156:157]
	v_lshlrev_b32_e32 v156, 4, v4
	v_lshl_add_u64 v[2:3], v[2:3], 0, v[156:157]
	v_add_co_u32_e64 v4, s[0:1], s0, v2
	v_lshl_or_b32 v1, s16, 4, v108
	s_nop 0
	v_addc_co_u32_e64 v5, s[0:1], 0, v3, s[0:1]
	s_movk_i32 s0, 0x2000
	s_nop 0
	v_add_co_u32_e64 v6, s[0:1], s0, v2
	v_or_b32_e32 v8, 8, v1
	s_nop 0
	v_addc_co_u32_e64 v7, s[0:1], 0, v3, s[0:1]
	s_add_u32 s0, s8, 0x30000
	v_mul_u32_u24_e32 v8, 0xc0, v8
	s_addc_u32 s1, s9, 0
	v_lshlrev_b32_e32 v8, 4, v8
	v_mul_u32_u24_e32 v1, 0xc0, v1
	v_lshl_add_u64 v[92:93], s[0:1], 0, v[8:9]
	v_lshlrev_b32_e32 v8, 4, v1
	s_cmp_lg_u32 s4, 0
	v_lshl_add_u64 v[8:9], s[0:1], 0, v[8:9]
	s_cselect_b64 s[12:13], -1, 0
	s_lshl_b32 s0, s16, 11
	s_add_u32 s0, s8, s0
	s_addc_u32 s1, s9, 0
	v_and_b32_e32 v10, 0x1c0, v0
	v_mov_b32_e32 v11, v157
	v_lshl_add_u64 v[10:11], s[0:1], 0, v[10:11]
	v_and_b32_e32 v12, 48, v0
	v_mov_b32_e32 v13, v157
	v_and_b32_e32 v161, 15, v0
	v_lshl_add_u64 v[10:11], v[10:11], 0, v[12:13]
	s_mov_b64 s[0:1], 0x48000
	v_lshrrev_b32_e32 v12, 5, v0
	v_bfe_u32 v13, v0, 5, 1
	v_bfe_u32 v109, v0, 4, 2
	v_lshl_add_u64 v[72:73], v[10:11], 0, s[0:1]
	s_mov_b32 s0, 0x48000
	v_lshlrev_b32_e32 v1, 3, v0
	v_and_or_b32 v12, v12, 2, v13
	v_lshlrev_b32_e32 v13, 4, v161
	v_lshrrev_b32_e32 v0, 1, v0
	v_add_co_u32_e64 v10, s[0:1], s0, v10
	v_and_b32_e32 v1, 0xc00, v1
	v_lshl_or_b32 v12, v12, 8, v13
	v_and_b32_e32 v0, 8, v0
	v_lshl_add_u64 v[8:9], v[8:9], 0, v[156:157]
	v_addc_co_u32_e64 v11, s[0:1], 0, v11, s[0:1]
	v_or3_b32 v163, v12, v1, v0
	global_load_dwordx4 v[12:15], v[2:3], off
	global_load_dwordx4 v[16:19], v[2:3], off offset:1024
	global_load_dwordx4 v[20:23], v[2:3], off offset:2048
	global_load_dwordx4 v[24:27], v[2:3], off offset:3072
	global_load_dwordx4 v[28:31], v[6:7], off offset:-4096
	global_load_dwordx4 v[32:35], v[6:7], off
	global_load_dwordx4 v[36:39], v[6:7], off offset:1024
	global_load_dwordx4 v[40:43], v[6:7], off offset:2048
	global_load_dwordx4 v[44:47], v[6:7], off offset:3072
	global_load_dwordx4 v[48:51], v[4:5], off offset:1024
	global_load_dwordx4 v[52:55], v[4:5], off offset:2048
	global_load_dwordx4 v[56:59], v[4:5], off offset:3072
	global_load_dwordx4 v[60:63], v[8:9], off
	global_load_dwordx4 v[64:67], v[8:9], off offset:1024
	global_load_dwordx4 v[68:71], v[8:9], off offset:2048
	global_load_dwordx4 v[76:79], v[72:73], off offset:512
	global_load_dwordx4 v[80:83], v[72:73], off offset:1024
	global_load_dwordx4 v[84:87], v[10:11], off
	global_load_dwordx4 v[88:91], v[72:73], off offset:1536
	s_and_b64 s[0:1], vcc, exec
	s_cselect_b32 s14, 0, 0x7f
	s_lshl_b32 s7, s16, 22
	s_add_u32 s0, s8, s7
	s_addc_u32 s1, s9, 0
	v_lshlrev_b32_e32 v94, 12, v108
	v_mov_b32_e32 v95, v157
	v_lshl_add_u64 v[0:1], s[0:1], 0, v[94:95]
	v_lshl_add_u64 v[0:1], v[0:1], 0, v[156:157]
	s_mov_b64 s[0:1], 0xc9000
	v_lshl_add_u64 v[158:159], v[0:1], 0, s[0:1]
	s_lshl_b32 s4, s14, 15
	v_lshl_add_u64 v[96:97], v[158:159], 0, s[4:5]
	global_load_dwordx4 v[72:75], v[96:97], off
	global_load_dwordx4 v[8:11], v[96:97], off offset:1024
	global_load_dwordx4 v[4:7], v[96:97], off offset:2048
	global_load_dwordx4 v[0:3], v[96:97], off offset:3072
	v_mul_u32_u24_e32 v95, 0x104, v161
	ds_read_b32 v96, v95 offset:16512
	ds_read_b32 v95, v95 offset:20672
	s_movk_i32 s6, 0x410
	s_movk_i32 s0, 0x104
	v_mov_b32_e32 v97, 0x4080
	s_waitcnt lgkmcnt(1)
	v_lshrrev_b32_e32 v178, 16, v96
	v_and_b32_e32 v96, 0xffff, v96
	v_mad_u32_u24 v176, v161, s0, v97
	v_mad_u32_u24 v110, v109, s6, v96
	s_waitcnt lgkmcnt(0)
	v_lshrrev_b32_e32 v177, 16, v95
	v_and_b32_e32 v95, 0xffff, v95
	s_and_b64 s[0:1], vcc, exec
	v_mad_u32_u24 v111, v109, s6, v95
	s_cselect_b32 s15, 1, -1
	s_or_b32 s0, s7, s4
	ds_read_b128 v[120:123], v110 offset:8192
	ds_read_b128 v[116:119], v111 offset:8192
	v_lshl_add_u64 v[164:165], v[92:93], 0, v[156:157]
	v_or3_b32 v92, s0, v94, v156
	v_mov_b32_e32 v93, v157
	v_lshl_add_u64 v[92:93], s[8:9], 0, v[92:93]
	s_mov_b64 s[0:1], 0xc9800
	s_lshl_b32 s4, s15, 1
	v_mov_b32_e32 v106, v157
	v_mov_b32_e32 v107, v157
	v_lshl_add_u64 v[166:167], v[92:93], 0, s[0:1]
	s_ashr_i32 s5, s4, 31
	v_mov_b32_e32 v100, 0xc47a0000
	v_mov_b32_e32 v104, v157
	v_mov_b32_e32 v105, v157
	v_cndmask_b32_e64 v92, 0, 1, s[12:13]
	v_mov_b64_e32 v[142:143], v[106:107]
	s_lshl_b64 s[6:7], s[4:5], 15
	s_add_i32 s8, s14, s15
	v_mov_b32_e32 v101, v100
	v_mov_b32_e32 v102, v100
	v_mov_b32_e32 v103, v100
	s_mov_b32 s5, -2
	v_cmp_ne_u32_e64 s[0:1], 1, v92
	v_mov_b32_e32 v172, v157
	v_mov_b32_e32 v173, v157
	v_mov_b32_e32 v174, v157
	v_mov_b32_e32 v175, v157
	v_mov_b32_e32 v96, v157
	v_mov_b32_e32 v97, v157
	v_mov_b32_e32 v98, v157
	v_mov_b32_e32 v99, v157
	v_mov_b32_e32 v92, v157
	v_mov_b32_e32 v93, v157
	v_mov_b32_e32 v94, v157
	v_mov_b32_e32 v95, v157
	v_mov_b32_e32 v144, v157
	v_mov_b32_e32 v145, v157
	v_mov_b32_e32 v146, v157
	v_mov_b32_e32 v147, v157
	v_mov_b32_e32 v132, v157
	v_mov_b32_e32 v133, v157
	v_mov_b32_e32 v134, v157
	v_mov_b32_e32 v135, v157
	v_mov_b32_e32 v128, v157
	v_mov_b32_e32 v129, v157
	v_mov_b32_e32 v130, v157
	v_mov_b32_e32 v131, v157
	v_mov_b32_e32 v136, v157
	v_mov_b32_e32 v137, v157
	v_mov_b32_e32 v138, v157
	v_mov_b32_e32 v139, v157
	v_mov_b32_e32 v124, v157
	v_mov_b32_e32 v125, v157
	v_mov_b32_e32 v126, v157
	v_mov_b32_e32 v127, v157
	v_mov_b32_e32 v170, v157
	v_mov_b32_e32 v171, v157
	v_mov_b32_e32 v168, v157
	v_mov_b32_e32 v169, v157
	v_lshlrev_b32_e32 v162, 4, v108
	v_mul_u32_u24_e32 v157, 0x410, v109
	v_lshlrev_b32_e32 v160, 2, v109
	v_mov_b64_e32 v[140:141], v[104:105]
	v_mov_b32_e32 v144, 0
	v_mov_b32_e32 v145, 0
	v_mov_b32_e32 v146, 0
	v_mov_b32_e32 v147, 0
	v_mov_b32_e32 v148, 0xc47a0000
	v_mov_b32_e32 v149, 0xc47a0000
	v_mov_b32_e32 v150, 0xc47a0000
	v_mov_b32_e32 v151, 0xc47a0000
	v_mov_b32_e32 v152, 0
	v_mov_b32_e32 v153, 0
	v_mov_b32_e32 v154, 0
	v_mov_b32_e32 v155, 0
	s_movk_i32 s17, 0x61
	global_load_dwordx4 v[206:209], v[164:165], off
	global_load_dwordx4 v[210:213], v[164:165], off offset:1024
	global_load_dwordx4 v[214:217], v[164:165], off offset:2048
	v_add_u32_e32 v252, v162, v160
	v_mul_u32_u24_e32 v252, 12, v252
	v_lshl_add_u32 v229, v161, 4, v157
	v_mul_u32_u24_e32 v230, 0x610, v161
	v_add_u32_e32 v230, v230, v252
	v_add_u32_e32 v231, 0x18400, v252
	s_waitcnt vmcnt(0) lgkmcnt(0)
	ds_read_b128 v[190:193], v229 offset:8192
	s_waitcnt lgkmcnt(0)
	v_mfma_f32_16x16x32_f16 v[194:197], v[60:63], v[190:193], v[84:87]
	v_mfma_f32_16x16x32_f16 v[198:201], v[64:67], v[190:193], v[76:79]
	v_mfma_f32_16x16x32_f16 v[202:205], v[68:71], v[190:193], v[88:91]
	s_nop 7
	s_nop 1
	ds_write_b128 v230, v[194:197] offset:24848
	ds_write_b128 v230, v[198:201] offset:24864
	ds_write_b128 v230, v[202:205] offset:24880
	v_add_u32_e32 v230, 0x6100, v230
	ds_read_b128 v[190:193], v229 offset:8448
	s_waitcnt lgkmcnt(0)
	v_mfma_f32_16x16x32_f16 v[194:197], v[60:63], v[190:193], v[84:87]
	v_mfma_f32_16x16x32_f16 v[198:201], v[64:67], v[190:193], v[76:79]
	v_mfma_f32_16x16x32_f16 v[202:205], v[68:71], v[190:193], v[88:91]
	s_nop 7
	s_nop 1
	ds_write_b128 v230, v[194:197] offset:24848
	ds_write_b128 v230, v[198:201] offset:24864
	ds_write_b128 v230, v[202:205] offset:24880
	v_add_u32_e32 v230, 0x6100, v230
	ds_read_b128 v[190:193], v229 offset:12864
	s_waitcnt lgkmcnt(0)
	v_mfma_f32_16x16x32_f16 v[194:197], v[206:209], v[190:193], v[84:87]
	v_mfma_f32_16x16x32_f16 v[198:201], v[210:213], v[190:193], v[76:79]
	v_mfma_f32_16x16x32_f16 v[202:205], v[214:217], v[190:193], v[88:91]
	s_nop 7
	s_nop 1
	ds_write_b128 v230, v[194:197] offset:24848
	ds_write_b128 v230, v[198:201] offset:24864
	ds_write_b128 v230, v[202:205] offset:24880
	v_add_u32_e32 v230, 0x6100, v230
	ds_read_b128 v[190:193], v229 offset:13120
	s_waitcnt lgkmcnt(0)
	v_mfma_f32_16x16x32_f16 v[194:197], v[206:209], v[190:193], v[84:87]
	v_mfma_f32_16x16x32_f16 v[198:201], v[210:213], v[190:193], v[76:79]
	v_mfma_f32_16x16x32_f16 v[202:205], v[214:217], v[190:193], v[88:91]
	s_nop 7
	s_nop 1
	ds_write_b128 v230, v[194:197] offset:24848
	ds_write_b128 v230, v[198:201] offset:24864
	ds_write_b128 v230, v[202:205] offset:24880
	ds_write_b128 v231, v[84:87] offset:24848
	ds_write_b128 v231, v[76:79] offset:24864
	ds_write_b128 v231, v[88:91] offset:24880
	ds_read_u16 v232, v176
	ds_read_u16 v177, v176 offset:4160
	s_waitcnt lgkmcnt(0)
	v_mad_u32_u24 v253, v232, s17, v252
	ds_read_b128 v[116:119], v253 offset:24848
	ds_read_b128 v[120:123], v253 offset:24864
	ds_read_b128 v[138:141], v253 offset:24880
	v_mov_b32_e32 v182, 0
	v_mov_b32_e32 v183, 0
	v_mov_b32_e32 v184, 0
	v_mov_b32_e32 v185, 0
	v_mov_b32_e32 v222, 0
	v_mov_b32_e32 v223, 0
	v_mov_b32_e32 v224, 0
	v_mov_b32_e32 v225, 0
	v_mov_b32_e32 v186, 0
	v_mov_b32_e32 v187, 0
	v_mov_b32_e32 v188, 0
	v_mov_b32_e32 v189, 0
	v_mov_b32_e32 v100, 0
	v_mov_b32_e32 v101, 0
	v_mov_b32_e32 v102, 0
	v_mov_b32_e32 v103, 0
	v_mov_b32_e32 v104, 0
	v_mov_b32_e32 v105, 0
	v_mov_b32_e32 v106, 0
	v_mov_b32_e32 v107, 0
	v_mov_b32_e32 v108, 0
	v_mov_b32_e32 v109, 0
	v_mov_b32_e32 v110, 0
	v_mov_b32_e32 v111, 0
	v_mov_b32_e32 v112, 0
	v_mov_b32_e32 v113, 0
	v_mov_b32_e32 v114, 0
	v_mov_b32_e32 v115, 0
	v_mov_b32_e32 v206, 0
	v_mov_b32_e32 v207, 0
	v_mov_b32_e32 v208, 0
	v_mov_b32_e32 v209, 0
	v_mov_b32_e32 v210, 0
	v_mov_b32_e32 v211, 0
	v_mov_b32_e32 v212, 0
	v_mov_b32_e32 v213, 0
	v_mov_b32_e32 v214, 0
	v_mov_b32_e32 v215, 0
	v_mov_b32_e32 v216, 0
	v_mov_b32_e32 v217, 0
	v_mov_b32_e32 v218, 0
	v_mov_b32_e32 v219, 0
	v_mov_b32_e32 v220, 0
	v_mov_b32_e32 v221, 0
	s_waitcnt vmcnt(4) lgkmcnt(0)
	v_readfirstlane_b32 s18, v162
	s_nop 3
	s_cmp_ge_u32 s18, 64
	s_cbranch_scc0 .Lgru_noprio
	s_setprio 1
.Lgru_noprio:
.Lgru_loop:
	ds_read_b128 v[190:193], v156 offset:0
	ds_read_b128 v[194:197], v156 offset:1024
	ds_read_b128 v[198:201], v156 offset:2048
	ds_read_b128 v[202:205], v156 offset:3072
	s_waitcnt vmcnt(4)
	v_mfma_f32_16x16x32_f16 v[92:95], v[112:115], v[206:209], v[92:95]
	v_exp_f32_e32 v228, v144
	v_exp_f32_e32 v229, v145
	v_exp_f32_e32 v230, v146
	v_mfma_f32_16x16x32_f16 v[92:95], v[108:111], v[210:213], v[92:95]
	v_exp_f32_e32 v231, v147
	v_exp_f32_e32 v232, v148
	v_exp_f32_e32 v233, v149
	v_mfma_f32_16x16x32_f16 v[92:95], v[104:107], v[214:217], v[92:95]
	v_exp_f32_e32 v234, v150
	v_exp_f32_e32 v235, v151
	v_add_f32_e32 v228, 1.0, v228
	v_add_f32_e32 v229, 1.0, v229
	v_mfma_f32_16x16x32_f16 v[92:95], v[100:103], v[218:221], v[92:95]
	global_load_dwordx4 v[112:115], v[166:167], off offset:-2048
	global_load_dwordx4 v[108:111], v[166:167], off offset:-1024
	global_load_dwordx4 v[104:107], v[166:167], off
	global_load_dwordx4 v[100:103], v[166:167], off offset:1024
	v_add_f32_e32 v230, 1.0, v230
	v_add_f32_e32 v231, 1.0, v231
	v_add_f32_e32 v232, 1.0, v232
	v_add_f32_e32 v233, 1.0, v233
	v_add_f32_e32 v234, 1.0, v234
	v_add_f32_e32 v235, 1.0, v235
	s_waitcnt lgkmcnt(3)
	v_mfma_f32_16x16x32_f16 v[124:127], v[12:15], v[190:193], v[116:119]
	v_rcp_f32_e32 v228, v228
	v_rcp_f32_e32 v229, v229
	v_rcp_f32_e32 v230, v230
	v_mfma_f32_16x16x32_f16 v[128:131], v[28:31], v[190:193], v[120:123]
	v_rcp_f32_e32 v231, v231
	v_fma_f32 v236, v228, v152, v182
	v_fma_f32 v237, v229, v153, v183
	v_fma_f32 v238, v230, v154, v184
	v_fma_f32 v239, v231, v155, v185
	v_mfma_f32_16x16x32_f16 v[132:135], v[32:35], v[190:193], v[80:83]
	v_mad_u32_u24 v253, v177, s17, v252
	ds_read_b128 v[222:225], v253 offset:24848
	ds_read_b128 v[186:189], v253 offset:24864
	ds_read_b128 v[182:185], v253 offset:24880
	ds_read_u16 v177, v176 offset:4162
	v_exp_f32_e32 v236, v236
	v_exp_f32_e32 v237, v237
	v_exp_f32_e32 v238, v238
	s_waitcnt lgkmcnt(6)
	v_mfma_f32_16x16x32_f16 v[124:127], v[16:19], v[194:197], v[124:127]
	v_exp_f32_e32 v239, v239
	v_rcp_f32_e32 v232, v232
	v_rcp_f32_e32 v233, v233
	v_mfma_f32_16x16x32_f16 v[128:131], v[48:51], v[194:197], v[128:131]
	v_rcp_f32_e32 v234, v234
	v_rcp_f32_e32 v235, v235
	v_add_f32_e32 v236, 1.0, v236
	v_add_f32_e32 v237, 1.0, v237
	v_mfma_f32_16x16x32_f16 v[132:135], v[36:39], v[194:197], v[132:135]
	v_add_f32_e32 v238, 1.0, v238
	v_add_f32_e32 v239, 1.0, v239
	v_rcp_f32_e32 v236, v236
	v_rcp_f32_e32 v237, v237
	s_waitcnt lgkmcnt(5)
	v_mfma_f32_16x16x32_f16 v[124:127], v[20:23], v[198:201], v[124:127]
	v_rcp_f32_e32 v238, v238
	v_rcp_f32_e32 v239, v239
	v_pk_fma_f32 v[236:237], v[236:237], -2.0, 1.0 op_sel_hi:[1,0,0]
	v_pk_fma_f32 v[238:239], v[238:239], -2.0, 1.0 op_sel_hi:[1,0,0]
	v_mfma_f32_16x16x32_f16 v[128:131], v[52:55], v[198:201], v[128:131]
	v_pk_add_f32 v[240:241], v[168:169], v[236:237] neg_lo:[0,1] neg_hi:[0,1]
	v_pk_add_f32 v[242:243], v[170:171], v[238:239] neg_lo:[0,1] neg_hi:[0,1]
	v_pk_fma_f32 v[168:169], v[232:233], v[240:241], v[236:237]
	v_pk_fma_f32 v[170:171], v[234:235], v[242:243], v[238:239]
	v_cvt_pk_f16_f32 v244, v168, v169
	v_cvt_pk_f16_f32 v245, v170, v171
	ds_write_b64 v163, v[244:245] offset:4096
	v_mfma_f32_16x16x32_f16 v[132:135], v[40:43], v[198:201], v[132:135]
	s_waitcnt lgkmcnt(5)
	v_mfma_f32_16x16x32_f16 v[124:127], v[24:27], v[202:205], v[124:127]
	v_mfma_f32_16x16x32_f16 v[128:131], v[56:59], v[202:205], v[128:131]
	v_mfma_f32_16x16x32_f16 v[132:135], v[44:47], v[202:205], v[132:135]
	s_waitcnt lgkmcnt(0)
	s_barrier
	ds_read_b128 v[206:209], v156 offset:4096
	ds_read_b128 v[210:213], v156 offset:5120
	ds_read_b128 v[214:217], v156 offset:6144
	ds_read_b128 v[218:221], v156 offset:7168
	s_waitcnt vmcnt(4)
	v_mfma_f32_16x16x32_f16 v[96:99], v[72:75], v[190:193], v[96:99]
	v_exp_f32_e32 v228, v124
	v_exp_f32_e32 v229, v125
	v_exp_f32_e32 v230, v126
	v_mfma_f32_16x16x32_f16 v[96:99], v[8:11], v[194:197], v[96:99]
	v_exp_f32_e32 v231, v127
	v_exp_f32_e32 v232, v128
	v_exp_f32_e32 v233, v129
	v_mfma_f32_16x16x32_f16 v[96:99], v[4:7], v[198:201], v[96:99]
	v_exp_f32_e32 v234, v130
	v_exp_f32_e32 v235, v131
	v_add_f32_e32 v228, 1.0, v228
	v_add_f32_e32 v229, 1.0, v229
	v_mfma_f32_16x16x32_f16 v[96:99], v[0:3], v[202:205], v[96:99]
	v_add_f32_e32 v230, 1.0, v230
	v_add_f32_e32 v231, 1.0, v231
	v_add_f32_e32 v232, 1.0, v232
	v_add_f32_e32 v233, 1.0, v233
	v_add_f32_e32 v234, 1.0, v234
	v_add_f32_e32 v235, 1.0, v235
	s_waitcnt lgkmcnt(3)
	v_mfma_f32_16x16x32_f16 v[144:147], v[12:15], v[206:209], v[222:225]
	v_rcp_f32_e32 v228, v228
	v_rcp_f32_e32 v229, v229
	v_rcp_f32_e32 v230, v230
	v_mfma_f32_16x16x32_f16 v[148:151], v[28:31], v[206:209], v[186:189]
	v_rcp_f32_e32 v231, v231
	v_fma_f32 v236, v228, v132, v138
	v_fma_f32 v237, v229, v133, v139
	v_fma_f32 v238, v230, v134, v140
	v_fma_f32 v239, v231, v135, v141
	v_mfma_f32_16x16x32_f16 v[152:155], v[32:35], v[206:209], v[80:83]
	v_mad_u32_u24 v253, v178, s17, v252
	ds_read_b128 v[116:119], v253 offset:24848
	ds_read_b128 v[120:123], v253 offset:24864
	ds_read_b128 v[138:141], v253 offset:24880
	ds_read_u16 v178, v176 offset:4
	v_exp_f32_e32 v236, v236
	v_exp_f32_e32 v237, v237
	v_exp_f32_e32 v238, v238
	s_waitcnt lgkmcnt(6)
	v_mfma_f32_16x16x32_f16 v[144:147], v[16:19], v[210:213], v[144:147]
	v_exp_f32_e32 v239, v239
	v_rcp_f32_e32 v232, v232
	v_rcp_f32_e32 v233, v233
	v_mfma_f32_16x16x32_f16 v[148:151], v[48:51], v[210:213], v[148:151]
	v_rcp_f32_e32 v234, v234
	v_rcp_f32_e32 v235, v235
	v_add_f32_e32 v236, 1.0, v236
	v_add_f32_e32 v237, 1.0, v237
	v_mfma_f32_16x16x32_f16 v[152:155], v[36:39], v[210:213], v[152:155]
	v_add_f32_e32 v238, 1.0, v238
	v_add_f32_e32 v239, 1.0, v239
	v_rcp_f32_e32 v236, v236
	v_rcp_f32_e32 v237, v237
	s_waitcnt lgkmcnt(5)
	v_mfma_f32_16x16x32_f16 v[144:147], v[20:23], v[214:217], v[144:147]
	v_rcp_f32_e32 v238, v238
	v_rcp_f32_e32 v239, v239
	v_pk_fma_f32 v[236:237], v[236:237], -2.0, 1.0 op_sel_hi:[1,0,0]
	v_pk_fma_f32 v[238:239], v[238:239], -2.0, 1.0 op_sel_hi:[1,0,0]
	v_mfma_f32_16x16x32_f16 v[148:151], v[52:55], v[214:217], v[148:151]
	v_pk_add_f32 v[240:241], v[172:173], v[236:237] neg_lo:[0,1] neg_hi:[0,1]
	v_pk_add_f32 v[242:243], v[174:175], v[238:239] neg_lo:[0,1] neg_hi:[0,1]
	v_pk_fma_f32 v[172:173], v[232:233], v[240:241], v[236:237]
	v_pk_fma_f32 v[174:175], v[234:235], v[242:243], v[238:239]
	v_cvt_pk_f16_f32 v244, v172, v173
	v_cvt_pk_f16_f32 v245, v174, v175
	ds_write_b64 v163, v[244:245]
	v_mfma_f32_16x16x32_f16 v[152:155], v[40:43], v[214:217], v[152:155]
	s_waitcnt lgkmcnt(5)
	v_mfma_f32_16x16x32_f16 v[144:147], v[24:27], v[218:221], v[144:147]
	v_mfma_f32_16x16x32_f16 v[148:151], v[56:59], v[218:221], v[148:151]
	v_mfma_f32_16x16x32_f16 v[152:155], v[44:47], v[218:221], v[152:155]
	s_waitcnt lgkmcnt(0)
	s_barrier
	ds_read_b128 v[190:193], v156 offset:0
	ds_read_b128 v[194:197], v156 offset:1024
	ds_read_b128 v[198:201], v156 offset:2048
	ds_read_b128 v[202:205], v156 offset:3072
	v_mfma_f32_16x16x32_f16 v[92:95], v[72:75], v[206:209], v[92:95]
	v_exp_f32_e32 v228, v144
	v_exp_f32_e32 v229, v145
	v_exp_f32_e32 v230, v146
	v_mfma_f32_16x16x32_f16 v[92:95], v[8:11], v[210:213], v[92:95]
	v_exp_f32_e32 v231, v147
	v_exp_f32_e32 v232, v148
	v_exp_f32_e32 v233, v149
	v_mfma_f32_16x16x32_f16 v[92:95], v[4:7], v[214:217], v[92:95]
	v_exp_f32_e32 v234, v150
	v_exp_f32_e32 v235, v151
	v_add_f32_e32 v228, 1.0, v228
	v_add_f32_e32 v229, 1.0, v229
	v_mfma_f32_16x16x32_f16 v[92:95], v[0:3], v[218:221], v[92:95]
	s_ashr_i32 s9, s8, 31
	s_lshl_b64 s[12:13], s[8:9], 15
	v_lshl_add_u64 v[246:247], v[158:159], 0, s[12:13]
	global_load_dwordx4 v[72:75], v[246:247], off
	global_load_dwordx4 v[8:11], v[246:247], off offset:1024
	global_load_dwordx4 v[4:7], v[246:247], off offset:2048
	global_load_dwordx4 v[0:3], v[246:247], off offset:3072
	v_add_f32_e32 v230, 1.0, v230
	v_add_f32_e32 v231, 1.0, v231
	v_add_f32_e32 v232, 1.0, v232
	v_add_f32_e32 v233, 1.0, v233
	v_add_f32_e32 v234, 1.0, v234
	v_add_f32_e32 v235, 1.0, v235
	s_waitcnt lgkmcnt(3)
	v_mfma_f32_16x16x32_f16 v[124:127], v[12:15], v[190:193], v[116:119]
	v_rcp_f32_e32 v228, v228
	v_rcp_f32_e32 v229, v229
	v_rcp_f32_e32 v230, v230
	v_mfma_f32_16x16x32_f16 v[128:131], v[28:31], v[190:193], v[120:123]
	v_rcp_f32_e32 v231, v231
	v_fma_f32 v236, v228, v152, v182
	v_fma_f32 v237, v229, v153, v183
	v_fma_f32 v238, v230, v154, v184
	v_fma_f32 v239, v231, v155, v185
	v_mfma_f32_16x16x32_f16 v[132:135], v[32:35], v[190:193], v[80:83]
	v_mad_u32_u24 v253, v177, s17, v252
	ds_read_b128 v[222:225], v253 offset:24848
	ds_read_b128 v[186:189], v253 offset:24864
	ds_read_b128 v[182:185], v253 offset:24880
	ds_read_u16 v177, v176 offset:4164
	v_exp_f32_e32 v236, v236
	v_exp_f32_e32 v237, v237
	v_exp_f32_e32 v238, v238
	s_waitcnt lgkmcnt(6)
	v_mfma_f32_16x16x32_f16 v[124:127], v[16:19], v[194:197], v[124:127]
	v_exp_f32_e32 v239, v239
	v_rcp_f32_e32 v232, v232
	v_rcp_f32_e32 v233, v233
	v_mfma_f32_16x16x32_f16 v[128:131], v[48:51], v[194:197], v[128:131]
	v_rcp_f32_e32 v234, v234
	v_rcp_f32_e32 v235, v235
	v_add_f32_e32 v236, 1.0, v236
	v_add_f32_e32 v237, 1.0, v237
	v_mfma_f32_16x16x32_f16 v[132:135], v[36:39], v[194:197], v[132:135]
	v_add_f32_e32 v238, 1.0, v238
	v_add_f32_e32 v239, 1.0, v239
	v_rcp_f32_e32 v236, v236
	v_rcp_f32_e32 v237, v237
	s_waitcnt lgkmcnt(5)
	v_mfma_f32_16x16x32_f16 v[124:127], v[20:23], v[198:201], v[124:127]
	v_rcp_f32_e32 v238, v238
	v_rcp_f32_e32 v239, v239
	v_pk_fma_f32 v[236:237], v[236:237], -2.0, 1.0 op_sel_hi:[1,0,0]
	v_pk_fma_f32 v[238:239], v[238:239], -2.0, 1.0 op_sel_hi:[1,0,0]
	v_mfma_f32_16x16x32_f16 v[128:131], v[52:55], v[198:201], v[128:131]
	v_pk_add_f32 v[240:241], v[168:169], v[236:237] neg_lo:[0,1] neg_hi:[0,1]
	v_pk_add_f32 v[242:243], v[170:171], v[238:239] neg_lo:[0,1] neg_hi:[0,1]
	v_pk_fma_f32 v[168:169], v[232:233], v[240:241], v[236:237]
	v_pk_fma_f32 v[170:171], v[234:235], v[242:243], v[238:239]
	v_cvt_pk_f16_f32 v244, v168, v169
	v_cvt_pk_f16_f32 v245, v170, v171
	ds_write_b64 v163, v[244:245] offset:4096
	v_mfma_f32_16x16x32_f16 v[132:135], v[40:43], v[198:201], v[132:135]
	s_waitcnt lgkmcnt(5)
	v_mfma_f32_16x16x32_f16 v[124:127], v[24:27], v[202:205], v[124:127]
	v_mfma_f32_16x16x32_f16 v[128:131], v[56:59], v[202:205], v[128:131]
	v_mfma_f32_16x16x32_f16 v[132:135], v[44:47], v[202:205], v[132:135]
	s_waitcnt lgkmcnt(0)
	s_barrier
	ds_read_b128 v[206:209], v156 offset:4096
	ds_read_b128 v[210:213], v156 offset:5120
	ds_read_b128 v[214:217], v156 offset:6144
	ds_read_b128 v[218:221], v156 offset:7168
	s_waitcnt vmcnt(4)
	v_mfma_f32_16x16x32_f16 v[96:99], v[112:115], v[190:193], v[96:99]
	v_exp_f32_e32 v228, v124
	v_exp_f32_e32 v229, v125
	v_exp_f32_e32 v230, v126
	v_mfma_f32_16x16x32_f16 v[96:99], v[108:111], v[194:197], v[96:99]
	v_exp_f32_e32 v231, v127
	v_exp_f32_e32 v232, v128
	v_exp_f32_e32 v233, v129
	v_mfma_f32_16x16x32_f16 v[96:99], v[104:107], v[198:201], v[96:99]
	v_exp_f32_e32 v234, v130
	v_exp_f32_e32 v235, v131
	v_add_f32_e32 v228, 1.0, v228
	v_add_f32_e32 v229, 1.0, v229
	v_mfma_f32_16x16x32_f16 v[96:99], v[100:103], v[202:205], v[96:99]
	v_add_f32_e32 v230, 1.0, v230
	v_add_f32_e32 v231, 1.0, v231
	v_add_f32_e32 v232, 1.0, v232
	v_add_f32_e32 v233, 1.0, v233
	v_add_f32_e32 v234, 1.0, v234
	v_add_f32_e32 v235, 1.0, v235
	s_waitcnt lgkmcnt(3)
	v_mfma_f32_16x16x32_f16 v[144:147], v[12:15], v[206:209], v[222:225]
	v_rcp_f32_e32 v228, v228
	v_rcp_f32_e32 v229, v229
	v_rcp_f32_e32 v230, v230
	v_mfma_f32_16x16x32_f16 v[148:151], v[28:31], v[206:209], v[186:189]
	v_rcp_f32_e32 v231, v231
	v_fma_f32 v236, v228, v132, v138
	v_fma_f32 v237, v229, v133, v139
	v_fma_f32 v238, v230, v134, v140
	v_fma_f32 v239, v231, v135, v141
	v_mfma_f32_16x16x32_f16 v[152:155], v[32:35], v[206:209], v[80:83]
	v_mad_u32_u24 v253, v178, s17, v252
	ds_read_b128 v[116:119], v253 offset:24848
	ds_read_b128 v[120:123], v253 offset:24864
	ds_read_b128 v[138:141], v253 offset:24880
	ds_read_u16 v178, v176 offset:6
	v_exp_f32_e32 v236, v236
	v_exp_f32_e32 v237, v237
	v_exp_f32_e32 v238, v238
	s_waitcnt lgkmcnt(6)
	v_mfma_f32_16x16x32_f16 v[144:147], v[16:19], v[210:213], v[144:147]
	v_exp_f32_e32 v239, v239
	v_rcp_f32_e32 v232, v232
	v_rcp_f32_e32 v233, v233
	v_mfma_f32_16x16x32_f16 v[148:151], v[48:51], v[210:213], v[148:151]
	v_rcp_f32_e32 v234, v234
	v_rcp_f32_e32 v235, v235
	v_add_f32_e32 v236, 1.0, v236
	v_add_f32_e32 v237, 1.0, v237
	v_mfma_f32_16x16x32_f16 v[152:155], v[36:39], v[210:213], v[152:155]
	v_add_f32_e32 v238, 1.0, v238
	v_add_f32_e32 v239, 1.0, v239
	v_rcp_f32_e32 v236, v236
	v_rcp_f32_e32 v237, v237
	s_waitcnt lgkmcnt(5)
	v_mfma_f32_16x16x32_f16 v[144:147], v[20:23], v[214:217], v[144:147]
	v_rcp_f32_e32 v238, v238
	v_rcp_f32_e32 v239, v239
	v_pk_fma_f32 v[236:237], v[236:237], -2.0, 1.0 op_sel_hi:[1,0,0]
	v_pk_fma_f32 v[238:239], v[238:239], -2.0, 1.0 op_sel_hi:[1,0,0]
	v_mfma_f32_16x16x32_f16 v[148:151], v[52:55], v[214:217], v[148:151]
	v_pk_add_f32 v[240:241], v[172:173], v[236:237] neg_lo:[0,1] neg_hi:[0,1]
	v_pk_add_f32 v[242:243], v[174:175], v[238:239] neg_lo:[0,1] neg_hi:[0,1]
	v_pk_fma_f32 v[172:173], v[232:233], v[240:241], v[236:237]
	v_pk_fma_f32 v[174:175], v[234:235], v[242:243], v[238:239]
	v_cvt_pk_f16_f32 v244, v172, v173
	v_cvt_pk_f16_f32 v245, v174, v175
	ds_write_b64 v163, v[244:245]
	v_mfma_f32_16x16x32_f16 v[152:155], v[40:43], v[214:217], v[152:155]
	s_waitcnt lgkmcnt(5)
	v_mfma_f32_16x16x32_f16 v[144:147], v[24:27], v[218:221], v[144:147]
	v_mfma_f32_16x16x32_f16 v[148:151], v[56:59], v[218:221], v[148:151]
	v_mfma_f32_16x16x32_f16 v[152:155], v[44:47], v[218:221], v[152:155]
	s_add_i32 s5, s5, 2
	s_add_i32 s8, s8, s4
	v_add_u32_e32 v176, 4, v176
	v_lshl_add_u64 v[166:167], v[166:167], 0, s[6:7]
	s_cmpk_gt_u32 s5, 0x7d
	s_waitcnt lgkmcnt(0)
	s_barrier
	s_cbranch_scc0 .Lgru_loop
	s_waitcnt vmcnt(0)
	v_mfma_f32_16x16x32_f16 v[92:95], v[112:115], v[206:209], v[92:95]
	v_mfma_f32_16x16x32_f16 v[92:95], v[108:111], v[210:213], v[92:95]
	v_mfma_f32_16x16x32_f16 v[92:95], v[104:107], v[214:217], v[92:95]
	v_mfma_f32_16x16x32_f16 v[92:95], v[100:103], v[218:221], v[92:95]
	ds_read_b128 v[190:193], v156 offset:0
	ds_read_b128 v[194:197], v156 offset:1024
	ds_read_b128 v[198:201], v156 offset:2048
	ds_read_b128 v[202:205], v156 offset:3072
	v_exp_f32_e32 v228, v144
	v_exp_f32_e32 v229, v145
	v_exp_f32_e32 v230, v146
	v_exp_f32_e32 v231, v147
	v_exp_f32_e32 v232, v148
	v_exp_f32_e32 v233, v149
	v_exp_f32_e32 v234, v150
	v_exp_f32_e32 v235, v151
	v_add_f32_e32 v228, 1.0, v228
	v_add_f32_e32 v229, 1.0, v229
	v_add_f32_e32 v230, 1.0, v230
	v_add_f32_e32 v231, 1.0, v231
	v_add_f32_e32 v232, 1.0, v232
	v_add_f32_e32 v233, 1.0, v233
	v_add_f32_e32 v234, 1.0, v234
	v_add_f32_e32 v235, 1.0, v235
	v_rcp_f32_e32 v228, v228
	v_rcp_f32_e32 v229, v229
	v_rcp_f32_e32 v230, v230
	v_rcp_f32_e32 v231, v231
	v_fma_f32 v236, v228, v152, v182
	v_fma_f32 v237, v229, v153, v183
	v_fma_f32 v238, v230, v154, v184
	v_fma_f32 v239, v231, v155, v185
	v_exp_f32_e32 v236, v236
	v_exp_f32_e32 v237, v237
	v_exp_f32_e32 v238, v238
	v_exp_f32_e32 v239, v239
	v_rcp_f32_e32 v232, v232
	v_rcp_f32_e32 v233, v233
	v_rcp_f32_e32 v234, v234
	v_rcp_f32_e32 v235, v235
	v_add_f32_e32 v236, 1.0, v236
	v_add_f32_e32 v237, 1.0, v237
	v_add_f32_e32 v238, 1.0, v238
	v_add_f32_e32 v239, 1.0, v239
	v_rcp_f32_e32 v236, v236
	v_rcp_f32_e32 v237, v237
	v_rcp_f32_e32 v238, v238
	v_rcp_f32_e32 v239, v239
	v_pk_fma_f32 v[236:237], v[236:237], -2.0, 1.0 op_sel_hi:[1,0,0]
	v_pk_fma_f32 v[238:239], v[238:239], -2.0, 1.0 op_sel_hi:[1,0,0]
	v_pk_add_f32 v[240:241], v[168:169], v[236:237] neg_lo:[0,1] neg_hi:[0,1]
	v_pk_add_f32 v[242:243], v[170:171], v[238:239] neg_lo:[0,1] neg_hi:[0,1]
	v_pk_fma_f32 v[168:169], v[232:233], v[240:241], v[236:237]
	v_pk_fma_f32 v[170:171], v[234:235], v[242:243], v[238:239]
	v_cvt_pk_f16_f32 v244, v168, v169
	v_cvt_pk_f16_f32 v245, v170, v171
	ds_write_b64 v163, v[244:245] offset:4096
	s_waitcnt lgkmcnt(1)
	v_mfma_f32_16x16x32_f16 v[96:99], v[72:75], v[190:193], v[96:99]
	v_mfma_f32_16x16x32_f16 v[96:99], v[8:11], v[194:197], v[96:99]
	v_mfma_f32_16x16x32_f16 v[96:99], v[4:7], v[198:201], v[96:99]
	v_mfma_f32_16x16x32_f16 v[96:99], v[0:3], v[202:205], v[96:99]
	s_waitcnt lgkmcnt(0)
	s_barrier
	ds_read_b128 v[206:209], v156 offset:4096
	ds_read_b128 v[210:213], v156 offset:5120
	ds_read_b128 v[214:217], v156 offset:6144
	ds_read_b128 v[218:221], v156 offset:7168
	s_lshl_b32 s0, s16, 21
	s_add_u32 s4, s10, s0
	s_addc_u32 s5, s11, 0
	s_lshl_b64 s[0:1], s[2:3], 9
	s_add_u32 s0, s4, s0
	s_addc_u32 s1, s5, s1
	v_lshlrev_b32_e32 v222, 9, v161
	v_mov_b32_e32 v223, 0
	v_lshlrev_b32_e32 v224, 2, v162
	v_mov_b32_e32 v225, 0
	v_lshl_add_u64 v[186:187], s[0:1], 0, v[224:225]
	v_lshlrev_b32_e32 v224, 2, v160
	v_lshl_add_u64 v[186:187], v[186:187], 0, v[224:225]
	v_lshl_add_u64 v[188:189], v[186:187], 0, v[222:223]
	v_or_b32_e32 v222, 0x2000, v222
	v_lshl_add_u64 v[246:247], v[186:187], 0, v[222:223]
	s_waitcnt lgkmcnt(0)
	v_mfma_f32_16x16x32_f16 v[92:95], v[72:75], v[206:209], v[92:95]
	v_mfma_f32_16x16x32_f16 v[92:95], v[8:11], v[210:213], v[92:95]
	v_mfma_f32_16x16x32_f16 v[92:95], v[4:7], v[214:217], v[92:95]
	v_mfma_f32_16x16x32_f16 v[92:95], v[0:3], v[218:221], v[92:95]
	s_nop 7
	s_nop 3
	global_store_dwordx4 v[188:189], v[96:99], off
	global_store_dwordx4 v[246:247], v[92:95], off
	s_endpgm
